# k17 + M3 padding rows gather the tile's own first pair (no pre-final H row is ever read) + M3 table build without the unused comb gather; arrival-time invalidate barriers
# baseline (speedup 1.0000x reference)
.LBB0_1185:
	s_or_b64 exec, exec, s[16:17]
	v_lshl_add_u32 v1, v206, 2, 0
	v_add_u32_e32 v2, 0x24200, v1
	s_waitcnt vmcnt(0)
	ds_write_b32 v2, v208
	v_cmp_lt_i32_e32 vcc, -1, v208
	v_mov_b32_e32 v2, 0
	s_and_saveexec_b64 s[16:17], vcc
	s_cbranch_execz .LBB0_1187
.LBB0_1187:
	s_or_b64 exec, exec, s[16:17]
	v_add_u32_e32 v1, 0x25a00, v1
	s_waitcnt vmcnt(0)
	ds_write_b32 v1, v2
	s_and_b64 exec, exec, s[2:3]
	s_cbranch_execz .LBB0_1189
	v_readlane_b32 s16, v255, 5
	v_mov_b32_e32 v1, s23
	v_mov_b32_e32 v2, s18
	v_mov_b32_e32 v3, s16
	ds_write_b96 v3, v[0:2]

.LBB0_1195:
	s_or_b64 exec, exec, s[16:17]
	v_lshl_add_u32 v1, v206, 2, 0
	v_add_u32_e32 v2, 0x24600, v1
	s_waitcnt vmcnt(0)
	ds_write_b32 v2, v208
	v_cmp_lt_i32_e32 vcc, -1, v208
	v_mov_b32_e32 v2, 0
	s_and_saveexec_b64 s[16:17], vcc
	s_cbranch_execz .LBB0_1197
.LBB0_1197:
	s_or_b64 exec, exec, s[16:17]
	v_add_u32_e32 v1, 0x25e00, v1
	s_waitcnt vmcnt(0)
	ds_write_b32 v1, v2
	s_and_b64 exec, exec, s[2:3]
	s_cbranch_execz .LBB0_1199
	v_readlane_b32 s16, v255, 6
	v_mov_b32_e32 v1, s24
	s_nop 0
	v_mov_b32_e32 v2, s16
	v_readlane_b32 s16, v255, 7
	ds_write2_b32 v2, v0, v1 offset1:1
	v_mov_b32_e32 v1, s23
	v_mov_b32_e32 v0, s16
	ds_write_b32 v0, v1

.LBB0_1205:
	s_or_b64 exec, exec, s[16:17]
	v_lshl_add_u32 v1, v206, 2, 0
	v_add_u32_e32 v2, 0x24a00, v1
	s_waitcnt vmcnt(0)
	ds_write_b32 v2, v208
	v_cmp_lt_i32_e32 vcc, -1, v208
	v_mov_b32_e32 v2, 0
	s_and_saveexec_b64 s[16:17], vcc
	s_cbranch_execz .LBB0_1207
.LBB0_1207:
	s_or_b64 exec, exec, s[16:17]
	v_add_u32_e32 v1, 0x26200, v1
	s_waitcnt vmcnt(0)
	ds_write_b32 v1, v2
	s_and_b64 exec, exec, s[2:3]
	s_cbranch_execz .LBB0_1209
	v_readlane_b32 s16, v255, 8
	v_mov_b32_e32 v1, s24
	s_nop 0
	v_mov_b32_e32 v2, s16
	v_readlane_b32 s16, v255, 9
	ds_write_b64 v2, v[0:1]
	v_mov_b32_e32 v1, s23
	v_mov_b32_e32 v0, s16
	ds_write_b32 v0, v1

.LBB0_1215:
	s_or_b64 exec, exec, s[16:17]
	v_lshl_add_u32 v1, v206, 2, 0
	v_add_u32_e32 v2, 0x24e00, v1
	s_waitcnt vmcnt(0)
	ds_write_b32 v2, v208
	v_cmp_lt_i32_e32 vcc, -1, v208
	v_mov_b32_e32 v2, 0
	s_and_saveexec_b64 s[16:17], vcc
	s_cbranch_execz .LBB0_1217
.LBB0_1217:
	s_or_b64 exec, exec, s[16:17]
	v_add_u32_e32 v1, 0x26600, v1
	s_waitcnt vmcnt(0)
	ds_write_b32 v1, v2
	s_and_b64 exec, exec, s[2:3]
	s_cbranch_execz .LBB0_1219
	v_readlane_b32 s16, v255, 10
	v_mov_b32_e32 v1, s24
	s_nop 0
	v_mov_b32_e32 v2, s16
	v_readlane_b32 s16, v255, 11
	ds_write2_b32 v2, v0, v1 offset1:1
	v_mov_b32_e32 v1, s23
	v_mov_b32_e32 v0, s16
	ds_write_b32 v0, v1

.LBB0_1225:
	s_or_b64 exec, exec, s[16:17]
	v_lshl_add_u32 v1, v206, 2, 0
	v_add_u32_e32 v2, 0x25200, v1
	s_waitcnt vmcnt(0)
	ds_write_b32 v2, v208
	v_cmp_lt_i32_e32 vcc, -1, v208
	v_mov_b32_e32 v2, 0
	s_and_saveexec_b64 s[16:17], vcc
	s_cbranch_execz .LBB0_1227
.LBB0_1227:
	s_or_b64 exec, exec, s[16:17]
	v_add_u32_e32 v1, 0x26a00, v1
	s_waitcnt vmcnt(0)
	ds_write_b32 v1, v2
	s_and_b64 exec, exec, s[2:3]
	s_cbranch_execz .LBB0_1229
	v_readlane_b32 s16, v255, 12
	v_mov_b32_e32 v1, s24
	v_mov_b32_e32 v2, s23
	v_mov_b32_e32 v3, s16
	ds_write_b96 v3, v[0:2]

.LBB0_1235:
	s_or_b64 exec, exec, s[16:17]
	v_lshl_add_u32 v1, v206, 2, 0
	v_add_u32_e32 v2, 0x25600, v1
	s_waitcnt vmcnt(0)
	ds_write_b32 v2, v208
	v_cmp_lt_i32_e32 vcc, -1, v208
	v_mov_b32_e32 v2, 0
	s_and_saveexec_b64 s[14:15], vcc
	s_cbranch_execz .LBB0_1237
.LBB0_1237:
	s_or_b64 exec, exec, s[14:15]
	v_add_u32_e32 v1, 0x26e00, v1
	s_waitcnt vmcnt(0)
	ds_write_b32 v1, v2

.LBB0_1254:
	s_lshl_b32 s10, s12, 4
	s_add_u32 s2, s8, 0x59140000
	s_addc_u32 s3, s9, 0
	s_lshl_b32 s50, s90, 25
	s_lshl_b64 s[14:15], s[50:51], 2
	s_add_u32 s16, s6, s14
	s_addc_u32 s17, s7, s15
	v_and_b32_e32 v3, 60, v206
	s_add_i32 s22, 0, 0x24200
	v_add_u32_e32 v200, s22, v3
	v_ashrrev_i32_e32 v3, 2, v206
	v_and_b32_e32 v201, -16, v3
	v_lshl_add_u32 v3, v201, 2, v200
	v_mov_b32_e32 v214, 0x24200
	ds_read_b32 v214, v214
	ds_read_b32 v3, v3
	v_add_u32_e32 v7, 0x2000, v4
	v_ashrrev_i32_e32 v7, 6, v7
	v_and_b32_e32 v202, -16, v7
	v_lshl_add_u32 v7, v202, 2, v200
	s_ashr_i32 s6, s5, 6
	ds_read_b32 v7, v7
	s_lshl_b32 s13, s6, 10
	s_waitcnt lgkmcnt(1)
	v_cmp_gt_i32_e32 vcc, 0, v3
	s_nop 1
	v_cndmask_b32_e32 v3, v3, v214, vcc
	v_and_b32_e32 v5, 32, v206
	v_and_b32_e32 v8, 48, v4
	v_lshlrev_b32_e32 v3, 10, v3
	s_add_i32 s13, s13, 0
	s_ashr_i32 s18, s5, 8
	s_and_b32 s19, s5, 0xc0
	v_bitop3_b32 v220, v3, v8, v5 bitop3:0xf6
	s_ashr_i32 s5, s4, 31
	s_mov_b32 m0, s13
	s_lshl_b32 s11, s18, 13
	s_lshl_b64 s[4:5], s[4:5], 22
	s_ashr_i32 s7, s6, 31
	global_load_lds_dwordx4 v220, s[2:3]
	s_add_i32 m0, s13, 0x2000
	s_waitcnt lgkmcnt(0)
	v_cmp_gt_i32_e32 vcc, 0, v7
	s_nop 1
	v_cndmask_b32_e32 v3, v7, v214, vcc
	s_add_u32 s14, s16, s4
	v_lshlrev_b32_e32 v3, 10, v3
	v_lshlrev_b32_e32 v2, 8, v2
	s_addc_u32 s15, s17, s5
	s_lshl_b64 s[4:5], s[6:7], 13
	v_and_b32_e32 v1, 63, v206
	v_bitop3_b32 v221, v3, v8, v5 bitop3:0xf6
	v_ashrrev_i32_e32 v3, 31, v2
	s_add_u32 s6, s14, s4
	v_lshlrev_b32_e32 v0, 2, v1
	s_addc_u32 s7, s15, s5
	v_lshlrev_b64 v[2:3], 2, v[2:3]
	v_xor_b32_e32 v6, 16, v0
	v_lshl_add_u64 v[2:3], s[6:7], 0, v[2:3]
	global_load_lds_dwordx4 v221, s[2:3]
	v_lshlrev_b32_e32 v208, 4, v1
	v_lshlrev_b32_e32 v8, 2, v6
	v_mov_b32_e32 v9, v209
	s_add_i32 m0, s13, 0x4000
	v_readfirstlane_b32 s6, v2
	v_readfirstlane_b32 s7, v3
	v_lshl_add_u64 v[198:199], v[2:3], 0, v[8:9]
	v_lshl_add_u64 v[196:197], v[2:3], 0, v[208:209]
	v_or_b32_e32 v1, 64, v220
	v_lshlrev_b32_e32 v7, 2, v206
	v_and_b32_e32 v7, 32, v7
	global_load_lds_dwordx4 v208, s[6:7]
	s_mov_b64 s[6:7], 0x10000
	v_lshl_add_u64 v[2:3], v[198:199], 0, s[6:7]
	s_add_i32 m0, s13, 0x6000
	s_mov_b64 s[6:7], 0x20000
	global_load_lds_dwordx4 v[2:3], off
	v_lshl_add_u64 v[2:3], v[196:197], 0, s[6:7]
	s_add_i32 m0, s13, 0x8000
	s_mov_b64 s[6:7], 0x30000
	global_load_lds_dwordx4 v[2:3], off
	v_lshl_add_u64 v[2:3], v[198:199], 0, s[6:7]
	s_add_i32 m0, s13, 0xa000
	s_mov_b64 s[6:7], 0x40000
	global_load_lds_dwordx4 v[2:3], off
	s_add_i32 m0, s13, 0xc000
	v_lshl_add_u64 v[2:3], v[196:197], 0, s[6:7]
	global_load_lds_dwordx4 v1, s[2:3]
	v_or_b32_e32 v1, 64, v221
	s_add_i32 m0, s13, 0xe000
	s_mov_b64 s[6:7], 0x50000
	global_load_lds_dwordx4 v1, s[2:3]
	s_add_i32 m0, s13, 0x10000
	v_and_b32_e32 v1, 15, v206
	global_load_lds_dwordx4 v[2:3], off
	v_lshl_add_u64 v[2:3], v[198:199], 0, s[6:7]
	s_add_i32 m0, s13, 0x12000
	s_mov_b64 s[6:7], 0x60000
	global_load_lds_dwordx4 v[2:3], off
	v_lshl_add_u64 v[2:3], v[196:197], 0, s[6:7]
	s_add_i32 m0, s13, 0x14000
	s_mov_b64 s[6:7], 0x70000
	global_load_lds_dwordx4 v[2:3], off
	v_lshl_add_u64 v[2:3], v[198:199], 0, s[6:7]
	s_add_i32 m0, s13, 0x16000
	s_add_u32 s16, s16, s4
	global_load_lds_dwordx4 v[2:3], off
	v_lshlrev_b32_e32 v3, 6, v1
	v_and_b32_e32 v2, 48, v206
	v_bitop3_b32 v203, v3, v7, v2 bitop3:0x36
	v_lshlrev_b32_e32 v3, 1, v1
	v_and_b32_e32 v7, 16, v206
	s_addc_u32 s17, s17, s5
	s_lshl_b32 s7, s18, 9
	s_lshl_b32 s4, s19, 1
	v_bitop3_b32 v3, s19, v7, v3 bitop3:0x36
	s_add_u32 s4, s8, s4
	v_lshlrev_b32_e32 v205, 2, v3
	s_addc_u32 s5, s9, 0
	v_mov_b32_e32 v3, v209
	v_lshlrev_b32_e32 v7, 9, v206
	v_lshl_add_u64 v[2:3], s[4:5], 0, v[2:3]
	s_mov_b64 s[4:5], 0x5a140000
	s_add_i32 s22, s22, s7
	s_mov_b32 s6, 2
	s_mov_b32 s14, 16
	v_and_b32_e32 v204, 0x6000, v7
	v_bitop3_b32 v206, v4, v5, 48 bitop3:0x6c
	s_mov_b32 s15, 0
	v_lshl_add_u64 v[192:193], v[2:3], 0, s[4:5]
	v_lshl_add_u32 v207, v1, 2, s22
	v_lshlrev_b32_e32 v208, 2, v0
	v_lshlrev_b32_e32 v194, 2, v6
	s_mov_b32 s18, 2
	s_mov_b32 s19, 2
	s_mov_b32 s22, 0
	s_mov_b32 s23, 0
	s_mov_b32 s24, 0
	s_branch .LBB0_1256

.LBB0_1257:
	v_lshl_add_u32 v196, s15, 10, v200
	v_lshl_add_u32 v197, v201, 2, v196
	v_lshl_add_u32 v196, v202, 2, v196
	s_lshl_b32 s100, s15, 10
	s_add_i32 s100, s100, 0x24200
	v_mov_b32_e32 v214, s100
	ds_read_b32 v214, v214
	ds_read_b32 v197, v197
	ds_read_b32 v196, v196
	s_ashr_i32 s5, s4, 31
	s_lshl_b64 s[4:5], s[4:5], 22
	s_add_u32 s4, s16, s4
	s_waitcnt lgkmcnt(1)
	v_cmp_gt_i32_e32 vcc, 0, v197
	s_nop 1
	v_cndmask_b32_e32 v197, v197, v214, vcc
	s_waitcnt lgkmcnt(0)
	v_cmp_gt_i32_e32 vcc, 0, v196
	s_nop 1
	v_cndmask_b32_e32 v196, v196, v214, vcc
	v_lshl_or_b32 v221, v196, 10, v206
	v_lshlrev_b32_e32 v196, 8, v195
	v_lshl_or_b32 v220, v197, 10, v206
	v_ashrrev_i32_e32 v197, 31, v196
	s_addc_u32 s5, s17, s5
	v_lshlrev_b64 v[196:197], 2, v[196:197]
	v_lshl_add_u64 v[198:199], s[4:5], 0, v[196:197]
	v_mov_b32_e32 v195, v209
	v_lshl_add_u64 v[196:197], v[198:199], 0, v[208:209]
	v_lshl_add_u64 v[198:199], v[198:199], 0, v[194:195]
